# grid barrier arrive/release rewritten by hand: all workgroups poll the top-level release word (no per-XCD release hop), generations counted in SGPRs (no divisions)
# baseline (speedup 1.0000x reference)
; #define LAS __attribute__((address_space(3)))
; __global__ void __launch_bounds__(NWAVES * 64, 2) mega(Args args) {
;     extern __shared__ __attribute__((aligned(16))) unsigned char lds[];
;     Frame F;
;     F.lds = (LAS unsigned char*)lds;
;     F.MISC = (volatile LAS unsigned*)(F.lds + MISC_OFF);
;     F.tid = threadIdx.x; F.lane = F.tid & 63; { int w_ = __builtin_amdgcn_readfirstlane(F.tid >> 6); asm volatile("" : "+s"(w_)); F.wave = w_; }
;     F.G = gridDim.x; { const int bx = blockIdx.x; F.vcu = (F.G % 8 == 0) ? (bx % 8) * (F.G / 8) + bx / 8 : bx; }
;     unsigned char* ws = args.ws;
;     F.ctl = (gu32*)(ws + WS_CTL);
;     for (int u = F.tid; u < (LDS_BYTES - LDSCTL_OFF) / 4; u += NWAVES * 64) ((LAS unsigned*)(F.lds + LDSCTL_OFF))[u] = 0u;
;     __syncthreads();
;     XcdBarrier bar; bar.bar = (unsigned*)(F.ctl + CW_BAR); bar.x = 0; bar.st = nullptr;
;     if (MK_ONE) bar = xcd_barrier_post((unsigned*)(F.ctl + CW_BAR), F.MISC + 8, F.wave);
_Z4mega4Args:
	s_mov_b32 s100, 0
	s_mov_b32 s101, 0
	s_load_dwordx2 s[30:31], s[0:1], 0x80
	s_load_dword s60, s[0:1], 0x90
	v_readfirstlane_b32 s3, v0
	s_lshr_b32 s61, s3, 6
	s_add_u32 s4, s0, 0x90
	s_addc_u32 s5, s1, 0
	s_waitcnt lgkmcnt(0)
	s_and_b32 s3, s60, 7
	v_writelane_b32 v248, s4, 0
	s_cmp_lg_u32 s3, 0
	s_mov_b32 s3, s2
	v_writelane_b32 v248, s5, 1
	s_cbranch_scc0 .LBB0_5
	s_movk_i32 s4, 0x80
	v_cmp_gt_u32_e32 vcc, s4, v0
	s_and_saveexec_b64 s[4:5], vcc

; __device__ __forceinline__ int mk_lane() { int l_ = (int)__builtin_amdgcn_mbcnt_hi(~0u, __builtin_amdgcn_mbcnt_lo(~0u, 0u)); asm volatile("" : "+v"(l_)); return l_; }
; __device__ __forceinline__ unsigned xb_ld(unsigned* p)              { return __hip_atomic_load(p, __ATOMIC_RELAXED, __HIP_MEMORY_SCOPE_AGENT); }
; __device__ __forceinline__ unsigned xb_add(unsigned* p, unsigned v) { return __hip_atomic_fetch_add(p, v, __ATOMIC_RELAXED, __HIP_MEMORY_SCOPE_AGENT); }
; #define XB_SPIN(cond, bar) do { unsigned _sp = 0; while (cond) { __builtin_amdgcn_s_sleep(1); \
;     if ((++_sp & 255u) == 0u) { if (xb_ld(&(bar)[XB_TMO])) break; if (_sp > XB_SPIN_CAP) { atomicAdd(&(bar)[XB_TMO], 1u); break; } } } } while (0)
; __device__ __forceinline__ void xcd_barrier(const XcdBarrier& b, int wave_id, int pair = -1) {
;     asm volatile("s_waitcnt vmcnt(0)" ::: "memory");
;     __syncthreads();
;     if (wave_id == 0 && mk_lane() == 0) {
;         unsigned* bar = b.bar;
;         __builtin_amdgcn_s_waitcnt(0);
;         unsigned nloc = b.st[0], nx = b.st[1];
;         if (nloc == 0u) { xcd_barrier_complete(bar, b.x, nloc, nx); b.st[0] = nloc; b.st[1] = nx; }
;         const unsigned old = xb_add(&bar[XB_XSUB(b.x)], 1u);
;         const unsigned gen = old / nloc;
;         if (old + 1u == (gen + 1u) * nloc) {
;             __builtin_amdgcn_fence(__ATOMIC_RELEASE, "agent");
;             asm volatile("s_waitcnt vmcnt(0)" ::: "memory");
;             unsigned* topw = pair < 0 ? &bar[XB_TOP] : &bar[XB_PTOP(pair)]; unsigned* topg = pair < 0 ? &bar[XB_TOPGEN] : &bar[XB_PTOPGEN(pair)];
;             if (pair >= 0) nx = 2u;
;             const unsigned og = xb_add(topw, 1u);
;             const unsigned tg = og / nx;
;             if (og + 1u == (tg + 1u) * nx) xb_add(topg, 1u);
;             else XB_SPIN(xb_ld(topg) == tg, bar);
;             __builtin_amdgcn_fence(__ATOMIC_ACQUIRE, "agent");
;             xb_add(&bar[XB_XGEN(b.x)], 1u);
;             asm volatile("s_waitcnt vmcnt(0)" ::: "memory");
;         } else {
;             XB_SPIN(xb_ld(&bar[XB_XGEN(b.x)]) == gen, bar);
;             __builtin_amdgcn_fence(__ATOMIC_ACQUIRE, "agent");
;             asm volatile("s_waitcnt vmcnt(0)" ::: "memory");
;         }
;     }
.LBB0_72:
	s_waitcnt lgkmcnt(0)
	v_readfirstlane_b32 s16, v2
	v_readfirstlane_b32 s17, v0
	s_add_u32 s8, s30, 0x4000
	s_addc_u32 s9, s31, 0
	s_lshl_b32 s12, s33, 8
	s_add_u32 s10, s8, s12
	s_addc_u32 s11, s9, 0
	s_movk_i32 s24, 0x3400
	s_movk_i32 s25, 0x3500
	s_mov_b32 s21, s100
	s_mov_b32 s22, 0
	s_add_u32 s12, s8, s24
	s_addc_u32 s13, s9, 0
	s_add_u32 s14, s8, s25
	s_addc_u32 s15, s9, 0
	s_add_i32 s18, s100, s101
	s_add_i32 s18, s18, 1
	s_mul_i32 s18, s18, s16
	v_mov_b32_e32 v1, 0
	v_mov_b32_e32 v3, 0x1000
	v_mov_b32_e32 v4, 1
	global_atomic_add v3, v3, v4, s[10:11] offset:1024 sc0
	s_waitcnt vmcnt(0)
	v_readfirstlane_b32 s19, v3
	s_add_i32 s19, s19, 1
	s_cmp_lg_u32 s19, s18
	s_cbranch_scc1 .Lxb0_nonleader
	buffer_wbl2 sc1
	buffer_inv sc1
	s_add_i32 s18, s21, 1
	s_mul_i32 s18, s18, s17
	s_waitcnt vmcnt(0)
	global_atomic_add v3, v1, v4, s[12:13] sc0
	s_waitcnt vmcnt(0)
	v_readfirstlane_b32 s19, v3
	s_add_i32 s19, s19, 1
	s_cmp_lg_u32 s19, s18
	s_cbranch_scc1 .Lxb0_spin
	global_atomic_add v1, v4, s[14:15]
	s_branch .Lxb0_done
.Lxb0_nonleader:
	buffer_inv sc1
.Lxb0_spin:
	s_mov_b32 s20, 0
.Lxb0_loop:
	global_load_dword v3, v1, s[14:15] sc1
	s_waitcnt vmcnt(0)
	v_readfirstlane_b32 s19, v3
	s_cmp_lg_u32 s19, s21
	s_cbranch_scc1 .Lxb0_done
	s_sleep 1
	s_add_i32 s20, s20, 1
	s_and_b32 s19, s20, 0xff
	s_cmp_lg_u32 s19, 0
	s_cbranch_scc1 .Lxb0_loop
	global_load_dword v3, v1, s[8:9] offset:512 sc1
	s_waitcnt vmcnt(0)
	v_readfirstlane_b32 s19, v3
	s_cmp_lg_u32 s19, 0
	s_cbranch_scc1 .Lxb0_done
	s_cmp_le_u32 s20, 0x40000
	s_cbranch_scc1 .Lxb0_loop
	global_atomic_add v1, v4, s[8:9] offset:512
.Lxb0_done:
	s_add_i32 s101, s101, s22
	s_xor_b32 s22, s22, 1
	s_add_i32 s100, s100, s22
	s_waitcnt vmcnt(0)

; __device__ __forceinline__ int mk_lane() { int l_ = (int)__builtin_amdgcn_mbcnt_hi(~0u, __builtin_amdgcn_mbcnt_lo(~0u, 0u)); asm volatile("" : "+v"(l_)); return l_; }
; __device__ __forceinline__ unsigned xb_ld(unsigned* p)              { return __hip_atomic_load(p, __ATOMIC_RELAXED, __HIP_MEMORY_SCOPE_AGENT); }
; __device__ __forceinline__ unsigned xb_add(unsigned* p, unsigned v) { return __hip_atomic_fetch_add(p, v, __ATOMIC_RELAXED, __HIP_MEMORY_SCOPE_AGENT); }
; __device__ __forceinline__ void xcd_barrier(const XcdBarrier& b, int wave_id, int pair = -1) {
;     asm volatile("s_waitcnt vmcnt(0)" ::: "memory");
;     __syncthreads();
;     if (wave_id == 0 && mk_lane() == 0) {
;         unsigned* bar = b.bar;
;         __builtin_amdgcn_s_waitcnt(0);
;         unsigned nloc = b.st[0], nx = b.st[1];
;         if (nloc == 0u) { xcd_barrier_complete(bar, b.x, nloc, nx); b.st[0] = nloc; b.st[1] = nx; }
;         const unsigned old = xb_add(&bar[XB_XSUB(b.x)], 1u);
;         const unsigned gen = old / nloc;
;         if (old + 1u == (gen + 1u) * nloc) {
;             __builtin_amdgcn_fence(__ATOMIC_RELEASE, "agent");
;             asm volatile("s_waitcnt vmcnt(0)" ::: "memory");
;             unsigned* topw = pair < 0 ? &bar[XB_TOP] : &bar[XB_PTOP(pair)]; unsigned* topg = pair < 0 ? &bar[XB_TOPGEN] : &bar[XB_PTOPGEN(pair)];
;             if (pair >= 0) nx = 2u;
;             const unsigned og = xb_add(topw, 1u);
;             const unsigned tg = og / nx;
;             if (og + 1u == (tg + 1u) * nx) xb_add(topg, 1u);
;             else XB_SPIN(xb_ld(topg) == tg, bar);
; template <int K> __device__ __forceinline__ void run_phase(Frame& F, const XcdBarrier& bar, int lo, int hi, unsigned char* lds) {
;     ...
;             constexpr bool PAIR_SEAM = MK_LOCALBAR && (sub == 0 || sub == 1);
;             bool pairok = false;
;             if (PAIR_SEAM) pairok = __hip_atomic_load((unsigned*)(F.ctl + CW_LBAR + 24 * 64), __ATOMIC_RELAXED, __HIP_MEMORY_SCOPE_AGENT) == 0u;
;             if (local) xcd_local_barrier((unsigned*)(F.ctl + CW_LBAR + ((sub == 2 ? l : 2) * 8 + (bx & 7)) * 64), (unsigned)(G >> 3), (unsigned*)(F.ctl + CW_BAR) + XB_TMO, F.wave);
;             else xcd_barrier(bar, F.wave, pairok ? ((bx & 7) >> 1) : -1);
.LBB0_209:
	s_waitcnt lgkmcnt(0)
	v_readfirstlane_b32 s16, v3
	v_readfirstlane_b32 s17, v1
	s_add_u32 s8, s30, 0x4000
	s_addc_u32 s9, s31, 0
	s_lshl_b32 s12, s33, 8
	s_add_u32 s10, s8, s12
	s_addc_u32 s11, s9, 0
	s_movk_i32 s24, 0x3400
	s_movk_i32 s25, 0x3500
	s_mov_b32 s21, s100
	s_mov_b32 s22, 0
	v_readfirstlane_b32 s23, v0
	s_cmp_lg_u32 s23, 0
	s_cbranch_scc1 .Lxb1_full
	s_lshl_b32 s23, s2, 7
	s_and_b32 s23, s23, 0x300
	s_add_i32 s24, s23, 0x3600
	s_add_i32 s25, s23, 0x3a00
	s_mov_b32 s17, 2
	s_mov_b32 s21, s101
	s_mov_b32 s22, 1
.Lxb1_full:
	s_add_u32 s12, s8, s24
	s_addc_u32 s13, s9, 0
	s_add_u32 s14, s8, s25
	s_addc_u32 s15, s9, 0
	s_add_i32 s18, s100, s101
	s_add_i32 s18, s18, 1
	s_mul_i32 s18, s18, s16
	v_mov_b32_e32 v2, 0
	v_mov_b32_e32 v4, 0x1000
	v_mov_b32_e32 v5, 1
	global_atomic_add v4, v4, v5, s[10:11] offset:1024 sc0
	s_waitcnt vmcnt(0)
	v_readfirstlane_b32 s19, v4
	s_add_i32 s19, s19, 1
	s_cmp_lg_u32 s19, s18
	s_cbranch_scc1 .Lxb1_nonleader
	buffer_wbl2 sc1
	buffer_inv sc1
	s_add_i32 s18, s21, 1
	s_mul_i32 s18, s18, s17
	s_waitcnt vmcnt(0)
	global_atomic_add v4, v2, v5, s[12:13] sc0
	s_waitcnt vmcnt(0)
	v_readfirstlane_b32 s19, v4
	s_add_i32 s19, s19, 1
	s_cmp_lg_u32 s19, s18
	s_cbranch_scc1 .Lxb1_spin
	global_atomic_add v2, v5, s[14:15]
	s_branch .Lxb1_done

; __device__ __forceinline__ unsigned xb_ld(unsigned* p)              { return __hip_atomic_load(p, __ATOMIC_RELAXED, __HIP_MEMORY_SCOPE_AGENT); }
; __device__ __forceinline__ unsigned xb_add(unsigned* p, unsigned v) { return __hip_atomic_fetch_add(p, v, __ATOMIC_RELAXED, __HIP_MEMORY_SCOPE_AGENT); }
; #define XB_SPIN(cond, bar) do { unsigned _sp = 0; while (cond) { __builtin_amdgcn_s_sleep(1); \
;     if ((++_sp & 255u) == 0u) { if (xb_ld(&(bar)[XB_TMO])) break; if (_sp > XB_SPIN_CAP) { atomicAdd(&(bar)[XB_TMO], 1u); break; } } } } while (0)
; __device__ __forceinline__ void xcd_barrier(const XcdBarrier& b, int wave_id, int pair = -1) {
;     ...
;             const unsigned tg = og / nx;
;             if (og + 1u == (tg + 1u) * nx) xb_add(topg, 1u);
;             else XB_SPIN(xb_ld(topg) == tg, bar);
;             __builtin_amdgcn_fence(__ATOMIC_ACQUIRE, "agent");
;             xb_add(&bar[XB_XGEN(b.x)], 1u);
;             asm volatile("s_waitcnt vmcnt(0)" ::: "memory");
;         } else {
;             XB_SPIN(xb_ld(&bar[XB_XGEN(b.x)]) == gen, bar);
;             __builtin_amdgcn_fence(__ATOMIC_ACQUIRE, "agent");
;             asm volatile("s_waitcnt vmcnt(0)" ::: "memory");
.Lxb1_loop:
	global_load_dword v4, v2, s[14:15] sc1
	s_waitcnt vmcnt(0)
	v_readfirstlane_b32 s19, v4
	s_cmp_lg_u32 s19, s21
	s_cbranch_scc1 .Lxb1_done
	s_sleep 1
	s_add_i32 s20, s20, 1
	s_and_b32 s19, s20, 0xff
	s_cmp_lg_u32 s19, 0
	s_cbranch_scc1 .Lxb1_loop
	global_load_dword v4, v2, s[8:9] offset:512 sc1
	s_waitcnt vmcnt(0)
	v_readfirstlane_b32 s19, v4
	s_cmp_lg_u32 s19, 0
	s_cbranch_scc1 .Lxb1_done
	s_cmp_le_u32 s20, 0x40000
	s_cbranch_scc1 .Lxb1_loop
	global_atomic_add v2, v5, s[8:9] offset:512
